# FFN-up GEMM k-loop: LDS-DMA stage loads issued in saddr form (SGPR base + 32-bit lane offset), dropping the 16 per-iteration 64-bit vector address adds
# speedup vs baseline: 1.0186x; 1.0034x over previous
.LBB0_1649:
	ds_read_b128 v[130:133], v167
	ds_read_b128 v[134:137], v167 offset:1024
	ds_read_b128 v[138:141], v167 offset:2048
	ds_read_b128 v[142:145], v167 offset:3072
	ds_read_b128 v[168:171], v228
	ds_read_b128 v[172:175], v228 offset:1024
	ds_read_b128 v[176:179], v228 offset:2048
	ds_read_b128 v[180:183], v228 offset:3072
	s_add_u32 s38, s34, 0xfff80080
	s_addc_u32 s39, s35, -1
	s_cmp_eq_u32 s77, 28
	s_cselect_b32 s45, s1, s39
	s_cselect_b32 s44, s29, s38
	s_cselect_b32 s43, s27, s47
	s_cselect_b32 s42, s41, s46
	s_add_i32 m0, s50, 0xc000
	ds_read_b128 v[184:187], v229
	ds_read_b128 v[188:191], v229 offset:1024
	ds_read_b128 v[192:195], v229 offset:2048
	ds_read_b128 v[196:199], v229 offset:3072
	ds_read_b128 v[200:203], v229 offset:4096
	ds_read_b128 v[204:207], v229 offset:5120
	ds_read_b128 v[208:211], v229 offset:6144
	ds_read_b128 v[212:215], v229 offset:7168
	global_load_lds_dwordx4 v158, s[34:35]
	s_add_i32 m0, s50, 0xe000
	s_nop 0
	global_load_lds_dwordx4 v160, s[34:35]
	s_waitcnt vmcnt(8)
	s_waitcnt lgkmcnt(0)
	s_barrier
	s_setprio 1
	s_waitcnt lgkmcnt(0)
	v_mfma_i32_16x16x64_i8 v[46:49], v[130:133], v[184:187], v[46:49]
	v_mfma_i32_16x16x64_i8 v[34:37], v[138:141], v[184:187], v[34:37]
	v_mfma_i32_16x16x64_i8 v[42:45], v[130:133], v[192:195], v[42:45]
	v_mfma_i32_16x16x64_i8 v[30:33], v[138:141], v[192:195], v[30:33]
	v_mfma_i32_16x16x64_i8 v[38:41], v[130:133], v[200:203], v[38:41]
	v_mfma_i32_16x16x64_i8 v[26:29], v[138:141], v[200:203], v[26:29]
	v_mfma_i32_16x16x64_i8 v[126:129], v[130:133], v[208:211], v[126:129]
	v_mfma_i32_16x16x64_i8 v[122:125], v[138:141], v[208:211], v[122:125]
	v_mfma_i32_16x16x64_i8 v[46:49], v[134:137], v[188:191], v[46:49]
	v_mfma_i32_16x16x64_i8 v[34:37], v[142:145], v[188:191], v[34:37]
	v_mfma_i32_16x16x64_i8 v[42:45], v[134:137], v[196:199], v[42:45]
	v_mfma_i32_16x16x64_i8 v[30:33], v[142:145], v[196:199], v[30:33]
	v_mfma_i32_16x16x64_i8 v[38:41], v[134:137], v[204:207], v[38:41]
	v_mfma_i32_16x16x64_i8 v[26:29], v[142:145], v[204:207], v[26:29]
	v_mfma_i32_16x16x64_i8 v[126:129], v[134:137], v[212:215], v[126:129]
	v_mfma_i32_16x16x64_i8 v[122:125], v[142:145], v[212:215], v[122:125]
	s_setprio 0
	s_setprio 1
	v_mfma_i32_16x16x64_i8 v[22:25], v[168:171], v[184:187], v[22:25]
	v_mfma_i32_16x16x64_i8 v[10:13], v[176:179], v[184:187], v[10:13]
	v_mfma_i32_16x16x64_i8 v[18:21], v[168:171], v[192:195], v[18:21]
	v_mfma_i32_16x16x64_i8 v[6:9], v[176:179], v[192:195], v[6:9]
	v_mfma_i32_16x16x64_i8 v[14:17], v[168:171], v[200:203], v[14:17]
	v_mfma_i32_16x16x64_i8 v[2:5], v[176:179], v[200:203], v[2:5]
	v_mfma_i32_16x16x64_i8 v[118:121], v[168:171], v[208:211], v[118:121]
	v_mfma_i32_16x16x64_i8 v[114:117], v[176:179], v[208:211], v[114:117]
	v_mfma_i32_16x16x64_i8 v[22:25], v[172:175], v[188:191], v[22:25]
	v_mfma_i32_16x16x64_i8 v[10:13], v[180:183], v[188:191], v[10:13]
	v_mfma_i32_16x16x64_i8 v[18:21], v[172:175], v[196:199], v[18:21]
	v_mfma_i32_16x16x64_i8 v[6:9], v[180:183], v[196:199], v[6:9]
	v_mfma_i32_16x16x64_i8 v[14:17], v[172:175], v[204:207], v[14:17]
	v_mfma_i32_16x16x64_i8 v[2:5], v[180:183], v[204:207], v[2:5]
	v_mfma_i32_16x16x64_i8 v[118:121], v[172:175], v[212:215], v[118:121]
	v_mfma_i32_16x16x64_i8 v[114:117], v[180:183], v[212:215], v[114:117]
	s_setprio 0
	s_barrier
	s_add_i32 s38, s64, s49
	s_mov_b32 m0, s38
	ds_read_b128 v[184:187], v229 offset:16384
	ds_read_b128 v[188:191], v229 offset:17408
	ds_read_b128 v[192:195], v229 offset:18432
	ds_read_b128 v[196:199], v229 offset:19456
	ds_read_b128 v[200:203], v229 offset:20480
	ds_read_b128 v[204:207], v229 offset:21504
	ds_read_b128 v[208:211], v229 offset:22528
	ds_read_b128 v[212:215], v229 offset:23552
	global_load_lds_dwordx4 v150, s[42:43]
	s_add_i32 m0, s38, 0x2000
	s_add_u32 s38, s42, 0x80000
	s_addc_u32 s39, s43, 0
	s_add_i32 s78, s65, s49
	global_load_lds_dwordx4 v154, s[42:43]
	s_mov_b32 m0, s78
	s_nop 0
	global_load_lds_dwordx4 v150, s[38:39]
	s_add_i32 m0, s78, 0x2000
	s_nop 0
	global_load_lds_dwordx4 v154, s[38:39]
	s_mov_b32 m0, s50
	s_nop 0
	global_load_lds_dwordx4 v148, s[44:45]
	s_mov_b32 m0, s51
	s_nop 0
	global_load_lds_dwordx4 v152, s[44:45]
	s_waitcnt vmcnt(8)
	s_waitcnt lgkmcnt(0)
	s_barrier
	s_setprio 1
	s_waitcnt lgkmcnt(0)
	v_mfma_i32_16x16x64_i8 v[94:97], v[130:133], v[184:187], v[94:97]
	v_mfma_i32_16x16x64_i8 v[70:73], v[138:141], v[184:187], v[70:73]
	v_mfma_i32_16x16x64_i8 v[86:89], v[130:133], v[192:195], v[86:89]
	v_mfma_i32_16x16x64_i8 v[62:65], v[138:141], v[192:195], v[62:65]
	v_mfma_i32_16x16x64_i8 v[78:81], v[130:133], v[200:203], v[78:81]
	v_mfma_i32_16x16x64_i8 v[54:57], v[138:141], v[200:203], v[54:57]
	v_mfma_i32_16x16x64_i8 v[110:113], v[130:133], v[208:211], v[110:113]
	v_mfma_i32_16x16x64_i8 v[106:109], v[138:141], v[208:211], v[106:109]
	v_mfma_i32_16x16x64_i8 v[94:97], v[134:137], v[188:191], v[94:97]
	v_mfma_i32_16x16x64_i8 v[70:73], v[142:145], v[188:191], v[70:73]
	v_mfma_i32_16x16x64_i8 v[86:89], v[134:137], v[196:199], v[86:89]
	v_mfma_i32_16x16x64_i8 v[62:65], v[142:145], v[196:199], v[62:65]
	v_mfma_i32_16x16x64_i8 v[78:81], v[134:137], v[204:207], v[78:81]
	v_mfma_i32_16x16x64_i8 v[54:57], v[142:145], v[204:207], v[54:57]
	v_mfma_i32_16x16x64_i8 v[110:113], v[134:137], v[212:215], v[110:113]
	v_mfma_i32_16x16x64_i8 v[106:109], v[142:145], v[212:215], v[106:109]
	s_setprio 0
	s_setprio 1
	v_mfma_i32_16x16x64_i8 v[90:93], v[168:171], v[184:187], v[90:93]
	v_mfma_i32_16x16x64_i8 v[66:69], v[176:179], v[184:187], v[66:69]
	v_mfma_i32_16x16x64_i8 v[82:85], v[168:171], v[192:195], v[82:85]
	v_mfma_i32_16x16x64_i8 v[58:61], v[176:179], v[192:195], v[58:61]
	v_mfma_i32_16x16x64_i8 v[74:77], v[168:171], v[200:203], v[74:77]
	v_mfma_i32_16x16x64_i8 v[50:53], v[176:179], v[200:203], v[50:53]
	v_mfma_i32_16x16x64_i8 v[102:105], v[168:171], v[208:211], v[102:105]
	v_mfma_i32_16x16x64_i8 v[98:101], v[176:179], v[208:211], v[98:101]
	v_mfma_i32_16x16x64_i8 v[90:93], v[172:175], v[188:191], v[90:93]
	v_mfma_i32_16x16x64_i8 v[66:69], v[180:183], v[188:191], v[66:69]
	v_mfma_i32_16x16x64_i8 v[82:85], v[172:175], v[196:199], v[82:85]
	v_mfma_i32_16x16x64_i8 v[58:61], v[180:183], v[196:199], v[58:61]
	v_mfma_i32_16x16x64_i8 v[74:77], v[172:175], v[204:207], v[74:77]
	v_mfma_i32_16x16x64_i8 v[50:53], v[180:183], v[204:207], v[50:53]
	v_mfma_i32_16x16x64_i8 v[102:105], v[172:175], v[212:215], v[102:105]
	v_mfma_i32_16x16x64_i8 v[98:101], v[180:183], v[212:215], v[98:101]
	s_setprio 0
	s_barrier
	s_add_i32 s78, 0, 0x18000
	s_add_i32 s79, 0, 0x1c000
	v_add_u32_e32 v142, s78, v1
	v_add_u32_e32 v156, s79, v1
	ds_read_b128 v[130:133], v142
	ds_read_b128 v[134:137], v142 offset:1024
	ds_read_b128 v[138:141], v142 offset:2048
	ds_read_b128 v[142:145], v142 offset:3072
	ds_read_b128 v[168:171], v156
	ds_read_b128 v[172:175], v156 offset:1024
	ds_read_b128 v[176:179], v156 offset:2048
	ds_read_b128 v[180:183], v156 offset:3072
	s_add_u32 s38, s44, 0x80000
	s_addc_u32 s39, s45, 0
	s_mov_b32 m0, s52
	ds_read_b128 v[184:187], v229 offset:32768
	ds_read_b128 v[188:191], v229 offset:33792
	ds_read_b128 v[192:195], v229 offset:34816
	ds_read_b128 v[196:199], v229 offset:35840
	ds_read_b128 v[200:203], v229 offset:36864
	ds_read_b128 v[204:207], v229 offset:37888
	ds_read_b128 v[208:211], v229 offset:38912
	ds_read_b128 v[212:215], v229 offset:39936
	global_load_lds_dwordx4 v148, s[38:39]
	s_mov_b32 m0, s53
	s_nop 0
	global_load_lds_dwordx4 v152, s[38:39]
	s_waitcnt vmcnt(8)
	s_waitcnt lgkmcnt(0)
	s_barrier
	s_setprio 1
	s_waitcnt lgkmcnt(0)
	v_mfma_i32_16x16x64_i8 v[46:49], v[130:133], v[184:187], v[46:49]
	v_mfma_i32_16x16x64_i8 v[34:37], v[138:141], v[184:187], v[34:37]
	v_mfma_i32_16x16x64_i8 v[42:45], v[130:133], v[192:195], v[42:45]
	v_mfma_i32_16x16x64_i8 v[30:33], v[138:141], v[192:195], v[30:33]
	v_mfma_i32_16x16x64_i8 v[38:41], v[130:133], v[200:203], v[38:41]
	v_mfma_i32_16x16x64_i8 v[26:29], v[138:141], v[200:203], v[26:29]
	v_mfma_i32_16x16x64_i8 v[126:129], v[130:133], v[208:211], v[126:129]
	v_mfma_i32_16x16x64_i8 v[122:125], v[138:141], v[208:211], v[122:125]
	v_mfma_i32_16x16x64_i8 v[46:49], v[134:137], v[188:191], v[46:49]
	v_mfma_i32_16x16x64_i8 v[34:37], v[142:145], v[188:191], v[34:37]
	v_mfma_i32_16x16x64_i8 v[42:45], v[134:137], v[196:199], v[42:45]
	v_mfma_i32_16x16x64_i8 v[30:33], v[142:145], v[196:199], v[30:33]
	v_mfma_i32_16x16x64_i8 v[38:41], v[134:137], v[204:207], v[38:41]
	v_mfma_i32_16x16x64_i8 v[26:29], v[142:145], v[204:207], v[26:29]
	v_mfma_i32_16x16x64_i8 v[126:129], v[134:137], v[212:215], v[126:129]
	v_mfma_i32_16x16x64_i8 v[122:125], v[142:145], v[212:215], v[122:125]
	s_setprio 0
	s_setprio 1
	v_mfma_i32_16x16x64_i8 v[22:25], v[168:171], v[184:187], v[22:25]
	v_mfma_i32_16x16x64_i8 v[10:13], v[176:179], v[184:187], v[10:13]
	v_mfma_i32_16x16x64_i8 v[18:21], v[168:171], v[192:195], v[18:21]
	v_mfma_i32_16x16x64_i8 v[6:9], v[176:179], v[192:195], v[6:9]
	v_mfma_i32_16x16x64_i8 v[14:17], v[168:171], v[200:203], v[14:17]
	v_mfma_i32_16x16x64_i8 v[2:5], v[176:179], v[200:203], v[2:5]
	v_mfma_i32_16x16x64_i8 v[118:121], v[168:171], v[208:211], v[118:121]
	v_mfma_i32_16x16x64_i8 v[114:117], v[176:179], v[208:211], v[114:117]
	v_mfma_i32_16x16x64_i8 v[22:25], v[172:175], v[188:191], v[22:25]
	v_mfma_i32_16x16x64_i8 v[10:13], v[180:183], v[188:191], v[10:13]
	v_mfma_i32_16x16x64_i8 v[18:21], v[172:175], v[196:199], v[18:21]
	v_mfma_i32_16x16x64_i8 v[6:9], v[180:183], v[196:199], v[6:9]
	v_mfma_i32_16x16x64_i8 v[14:17], v[172:175], v[204:207], v[14:17]
	v_mfma_i32_16x16x64_i8 v[2:5], v[180:183], v[204:207], v[2:5]
	v_mfma_i32_16x16x64_i8 v[118:121], v[172:175], v[212:215], v[118:121]
	v_mfma_i32_16x16x64_i8 v[114:117], v[180:183], v[212:215], v[114:117]
	s_setprio 0
	s_barrier
	s_add_i32 s38, s78, s49
	s_add_u32 s98, s42, s14
	s_addc_u32 s99, s43, s15
	s_add_u32 s100, s44, s14
	s_addc_u32 s101, s45, s15
	s_mov_b32 m0, s38
	ds_read_b128 v[184:187], v229 offset:49152
	ds_read_b128 v[188:191], v229 offset:50176
	ds_read_b128 v[192:195], v229 offset:51200
	ds_read_b128 v[196:199], v229 offset:52224
	ds_read_b128 v[200:203], v229 offset:53248
	ds_read_b128 v[204:207], v229 offset:54272
	ds_read_b128 v[208:211], v229 offset:55296
	ds_read_b128 v[212:215], v229 offset:56320
	global_load_lds_dwordx4 v150, s[98:99]
	s_add_i32 m0, s38, 0x2000
	s_add_u32 s38, s42, 0x80080
	s_addc_u32 s39, s43, 0
	s_add_i32 s42, s79, s49
	global_load_lds_dwordx4 v154, s[98:99]
	s_mov_b32 m0, s42
	s_nop 0
	global_load_lds_dwordx4 v150, s[38:39]
	s_add_i32 m0, s42, 0x2000
	s_nop 0
	global_load_lds_dwordx4 v154, s[38:39]
	s_mov_b32 m0, s57
	s_nop 0
	global_load_lds_dwordx4 v148, s[100:101]
	s_mov_b32 m0, s58
	s_nop 0
	global_load_lds_dwordx4 v152, s[100:101]
	s_waitcnt vmcnt(8)
	s_waitcnt lgkmcnt(0)
	s_barrier
	s_setprio 1
	s_waitcnt lgkmcnt(0)
	v_mfma_i32_16x16x64_i8 v[94:97], v[130:133], v[184:187], v[94:97]
	v_mfma_i32_16x16x64_i8 v[70:73], v[138:141], v[184:187], v[70:73]
	v_mfma_i32_16x16x64_i8 v[86:89], v[130:133], v[192:195], v[86:89]
	v_mfma_i32_16x16x64_i8 v[62:65], v[138:141], v[192:195], v[62:65]
	v_mfma_i32_16x16x64_i8 v[78:81], v[130:133], v[200:203], v[78:81]
	v_mfma_i32_16x16x64_i8 v[54:57], v[138:141], v[200:203], v[54:57]
	v_mfma_i32_16x16x64_i8 v[110:113], v[130:133], v[208:211], v[110:113]
	v_mfma_i32_16x16x64_i8 v[106:109], v[138:141], v[208:211], v[106:109]
	v_mfma_i32_16x16x64_i8 v[94:97], v[134:137], v[188:191], v[94:97]
	v_mfma_i32_16x16x64_i8 v[70:73], v[142:145], v[188:191], v[70:73]
	v_mfma_i32_16x16x64_i8 v[86:89], v[134:137], v[196:199], v[86:89]
	v_mfma_i32_16x16x64_i8 v[62:65], v[142:145], v[196:199], v[62:65]
	v_mfma_i32_16x16x64_i8 v[78:81], v[134:137], v[204:207], v[78:81]
	v_mfma_i32_16x16x64_i8 v[54:57], v[142:145], v[204:207], v[54:57]
	v_mfma_i32_16x16x64_i8 v[110:113], v[134:137], v[212:215], v[110:113]
	v_mfma_i32_16x16x64_i8 v[106:109], v[142:145], v[212:215], v[106:109]
	s_setprio 0
	s_setprio 1
	v_mfma_i32_16x16x64_i8 v[90:93], v[168:171], v[184:187], v[90:93]
	v_mfma_i32_16x16x64_i8 v[66:69], v[176:179], v[184:187], v[66:69]
	v_mfma_i32_16x16x64_i8 v[82:85], v[168:171], v[192:195], v[82:85]
	v_mfma_i32_16x16x64_i8 v[58:61], v[176:179], v[192:195], v[58:61]
	v_mfma_i32_16x16x64_i8 v[74:77], v[168:171], v[200:203], v[74:77]
	v_mfma_i32_16x16x64_i8 v[50:53], v[176:179], v[200:203], v[50:53]
	v_mfma_i32_16x16x64_i8 v[102:105], v[168:171], v[208:211], v[102:105]
	v_mfma_i32_16x16x64_i8 v[98:101], v[176:179], v[208:211], v[98:101]
	v_mfma_i32_16x16x64_i8 v[90:93], v[172:175], v[188:191], v[90:93]
	v_mfma_i32_16x16x64_i8 v[66:69], v[180:183], v[188:191], v[66:69]
	v_mfma_i32_16x16x64_i8 v[82:85], v[172:175], v[196:199], v[82:85]
	v_mfma_i32_16x16x64_i8 v[58:61], v[180:183], v[196:199], v[58:61]
	v_mfma_i32_16x16x64_i8 v[74:77], v[172:175], v[204:207], v[74:77]
	v_mfma_i32_16x16x64_i8 v[50:53], v[180:183], v[204:207], v[50:53]
	v_mfma_i32_16x16x64_i8 v[102:105], v[172:175], v[212:215], v[102:105]
	v_mfma_i32_16x16x64_i8 v[98:101], v[180:183], v[212:215], v[98:101]
	s_setprio 0
	s_barrier
	s_add_i32 s77, s77, 2
	s_add_u32 s34, s34, 0x100
	s_addc_u32 s35, s35, 0
	s_add_u32 s46, s46, 0x100
	s_addc_u32 s47, s47, 0
	s_cmp_gt_u32 s77, 29
	s_cbranch_scc0 .LBB0_1649
	s_and_b64 vcc, exec, s[16:17]
	s_cbranch_vccz .LBB0_1652
	s_barrier
